# state update: scalar, ws*V, ws reads and first three K^T fragments issued right after barrier 3, ahead of the h-output arithmetic
# speedup vs baseline: 1.0042x; 1.0014x over previous
.LBB0_734:
	s_or_b64 exec, exec, s[80:81]
	v_cndmask_b32_e64 v171, v79, v87, s[62:63]
	v_cndmask_b32_e64 v170, v78, v86, s[62:63]
	v_cndmask_b32_e64 v169, v77, v85, s[62:63]
	v_cndmask_b32_e64 v168, v76, v84, s[62:63]
	v_cndmask_b32_e64 v172, v80, v88, s[62:63]
	v_add_u32_e32 v0, s11, v131
	v_cndmask_b32_e64 v175, v83, v91, s[62:63]
	v_cndmask_b32_e64 v174, v82, v90, s[62:63]
	v_cndmask_b32_e64 v173, v81, v89, s[62:63]
	ds_write_b128 v0, v[168:171]
	ds_write_b128 v0, v[172:175] offset:1024
	v_cndmask_b32_e64 v172, v84, v76, s[62:63]
	v_add_u32_e32 v76, s21, v131
	s_waitcnt lgkmcnt(0)
	s_barrier
	v_mov_b32_e32 v226, s19
	ds_read_b32 v222, v226
	v_bfe_u32 v223, v110, 4, 2
	v_mul_u32_u24_e32 v226, 0x90, v223
	v_add_u32_e32 v226, v226, v167
	v_add_u32_e32 v227, 0x13e00, v226
	v_add_u32_e32 v226, 0x12c00, v226
	ds_read_b64_tr_b16 v[210:211], v226
	ds_read_b64_tr_b16 v[212:213], v226 offset:144
	ds_read_b128 v[214:217], v135
	ds_read_b128 v[218:221], v135 offset:16
	ds_read_b64_tr_b16 v[206:207], v227
	ds_read_b64_tr_b16 v[208:209], v227 offset:144
	v_mul_u32_u24_e32 v223, 0x210, v223
	v_add_u32_e32 v224, v223, v2
	ds_read_b128 v[198:201], v135 offset:128
	ds_read_b128 v[202:205], v135 offset:144
	s_mov_b32 s98, 0
	s_and_b64 vcc, exec, s[28:29]
	s_cselect_b32 s98, 64, s98
	s_and_b64 vcc, exec, s[30:31]
	s_cselect_b32 s98, 0x80, s98
	s_and_b64 vcc, exec, s[34:35]
	s_cselect_b32 s98, 0xc0, s98
	v_add_u32_e32 v225, s98, v224
	ds_read_b64_tr_b16 v[232:233], v224
	ds_read_b64_tr_b16 v[234:235], v224 offset:528
	ds_read_b64_tr_b16 v[236:237], v224 offset:32
	ds_read_b64_tr_b16 v[238:239], v224 offset:560
	ds_read_b64_tr_b16 v[240:241], v224 offset:64
	ds_read_b64_tr_b16 v[242:243], v224 offset:592
	v_cndmask_b32_e64 v0, v87, v79, s[62:63]
	v_cndmask_b32_e64 v3, v86, v78, s[62:63]
	v_cndmask_b32_e64 v178, v85, v77, s[62:63]
	v_cndmask_b32_e64 v179, v91, v83, s[62:63]
	v_cndmask_b32_e64 v180, v90, v82, s[62:63]
	v_cndmask_b32_e64 v181, v89, v81, s[62:63]
	v_cndmask_b32_e64 v182, v88, v80, s[62:63]
	ds_read_b128 v[80:83], v76
	ds_read_b128 v[76:79], v76 offset:1024
	ds_read_b128 v[84:87], v159
	ds_read_b128 v[88:91], v160
	ds_read_b128 v[168:171], v161
	s_waitcnt lgkmcnt(4)
	v_add_f32_e32 v80, v172, v80
	v_lshl_add_u64 v[174:175], v[104:105], 0, s[88:89]
	s_waitcnt lgkmcnt(2)
	v_fma_f32 v80, v80, v84, v92
	s_waitcnt lgkmcnt(1)
	v_max_f32_e64 v88, |v88|, |v88|
	s_waitcnt lgkmcnt(0)
	v_max_f32_e32 v84, v168, v168
	v_max_f32_e32 v84, v88, v84
	v_div_scale_f32 v88, s[80:81], v84, v84, v80
	v_rcp_f32_e32 v92, v88
	s_mov_b32 s80, 0x3a800000
	v_add_f32_e32 v3, v3, v82
	v_fma_f32 v3, v3, v86, v94
	v_fma_f32 v168, -v88, v92, 1.0
	v_fmac_f32_e32 v92, v168, v92
	v_div_scale_f32 v168, vcc, v80, v84, v80
	v_mul_f32_e32 v172, v168, v92
	v_fma_f32 v173, -v88, v172, v168
	v_fmac_f32_e32 v172, v173, v92
	v_fma_f32 v88, -v88, v172, v168
	v_div_fmas_f32 v88, v88, v92, v172
	v_div_fixup_f32 v80, v88, v84, v80
	v_add_co_u32_e32 v176, vcc, s80, v174
	v_cvt_pk_bf16_f32 v80, v80, v1
	v_max_f32_e64 v84, |v89|, |v89|
	s_nop 0
	v_addc_co_u32_e32 v177, vcc, 0, v175, vcc
	global_store_short v[176:177], v80, off
	v_add_f32_e32 v80, v178, v81
	v_max_f32_e32 v81, v169, v169
	v_fma_f32 v80, v80, v85, v93
	v_max_f32_e32 v81, v84, v81
	v_div_scale_f32 v84, s[80:81], v81, v81, v80
	v_rcp_f32_e32 v85, v84
	v_lshl_add_u64 v[172:173], v[106:107], 0, s[88:89]
	v_add_f32_e32 v0, v0, v83
	v_fmac_f32_e32 v95, v0, v87
	v_fma_f32 v88, -v84, v85, 1.0
	v_fmac_f32_e32 v85, v88, v85
	v_div_scale_f32 v88, vcc, v80, v81, v80
	v_mul_f32_e32 v89, v88, v85
	v_fma_f32 v92, -v84, v89, v88
	v_fmac_f32_e32 v89, v92, v85
	v_fma_f32 v84, -v84, v89, v88
	v_div_fmas_f32 v84, v84, v85, v89
	v_div_fixup_f32 v80, v84, v81, v80
	v_cvt_pk_bf16_f32 v84, v80, v1
	v_or_b32_e32 v80, 0x800, v172
	v_mov_b32_e32 v81, v173
	v_lshl_add_u64 v[80:81], v[102:103], 0, v[80:81]
	global_store_short v[80:81], v84, off
	v_max_f32_e32 v80, v170, v170
	v_max_f32_e64 v81, |v90|, |v90|
	v_max_f32_e32 v80, v81, v80
	v_div_scale_f32 v81, s[80:81], v80, v80, v3
	v_rcp_f32_e32 v82, v81
	v_max_f32_e32 v0, v171, v171
	v_lshl_add_u64 v[92:93], v[172:173], 0, s[96:97]
	v_fma_f32 v84, -v81, v82, 1.0
	v_fmac_f32_e32 v82, v84, v82
	v_div_scale_f32 v84, vcc, v3, v80, v3
	v_mul_f32_e32 v85, v84, v82
	v_fma_f32 v86, -v81, v85, v84
	v_fmac_f32_e32 v85, v86, v82
	v_fma_f32 v81, -v81, v85, v84
	v_div_fmas_f32 v81, v81, v82, v85
	v_div_fixup_f32 v3, v81, v80, v3
	v_or_b32_e32 v80, 0x1000, v172
	v_mov_b32_e32 v81, v173
	v_cvt_pk_bf16_f32 v3, v3, v1
	v_lshl_add_u64 v[80:81], v[102:103], 0, v[80:81]
	global_store_short v[80:81], v3, off
	v_max_f32_e64 v3, |v91|, |v91|
	v_max_f32_e32 v0, v3, v0
	v_div_scale_f32 v3, s[80:81], v0, v0, v95
	v_rcp_f32_e32 v80, v3
	s_nop 0
	v_fma_f32 v81, -v3, v80, 1.0
	v_fmac_f32_e32 v80, v81, v80
	v_div_scale_f32 v81, vcc, v95, v0, v95
	v_mul_f32_e32 v82, v81, v80
	v_fma_f32 v83, -v3, v82, v81
	v_fmac_f32_e32 v82, v83, v80
	v_fma_f32 v3, -v3, v82, v81
	v_div_fmas_f32 v3, v3, v80, v82
	v_or_b32_e32 v80, 0x1800, v172
	v_mov_b32_e32 v81, v173
	v_div_fixup_f32 v0, v3, v0, v95
	v_lshl_add_u64 v[80:81], v[102:103], 0, v[80:81]
	v_cvt_pk_bf16_f32 v0, v0, v1
	global_store_short v[80:81], v0, off
	ds_read_b128 v[80:83], v159 offset:64
	ds_read_b128 v[84:87], v160 offset:64
	ds_read_b128 v[88:91], v161 offset:64
	v_add_f32_e32 v0, v182, v76
	s_waitcnt lgkmcnt(0)
	v_fma_f32 v0, v0, v80, v72
	v_max_f32_e64 v72, |v84|, |v84|
	v_max_f32_e32 v3, v88, v88
	v_max_f32_e32 v3, v72, v3
	v_div_scale_f32 v72, s[80:81], v3, v3, v0
	v_rcp_f32_e32 v76, v72
	s_mov_b32 s80, 0x3a808000
	v_fma_f32 v80, -v72, v76, 1.0
	v_fmac_f32_e32 v76, v80, v76
	v_div_scale_f32 v80, vcc, v0, v3, v0
	v_mul_f32_e32 v84, v80, v76
	v_fma_f32 v88, -v72, v84, v80
	v_fmac_f32_e32 v84, v88, v76
	v_fma_f32 v72, -v72, v84, v80
	v_div_fmas_f32 v72, v72, v76, v84
	v_div_fixup_f32 v0, v72, v3, v0
	v_add_co_u32_e32 v94, vcc, s80, v174
	v_cvt_pk_bf16_f32 v0, v0, v1
	v_max_f32_e32 v3, v89, v89
	s_nop 0
	v_addc_co_u32_e32 v95, vcc, 0, v175, vcc
	global_store_short v[94:95], v0, off
	v_add_f32_e32 v0, v181, v77
	v_max_f32_e64 v72, |v85|, |v85|
	v_fma_f32 v0, v0, v81, v73
	v_max_f32_e32 v3, v72, v3
	v_div_scale_f32 v72, s[80:81], v3, v3, v0
	v_rcp_f32_e32 v73, v72
	v_add_u32_e32 v94, 0, v2
	v_fma_f32 v76, -v72, v73, 1.0
	v_fmac_f32_e32 v73, v76, v73
	v_div_scale_f32 v76, vcc, v0, v3, v0
	v_mul_f32_e32 v77, v76, v73
	v_fma_f32 v80, -v72, v77, v76
	v_fmac_f32_e32 v77, v80, v73
	v_fma_f32 v72, -v72, v77, v76
	v_div_fmas_f32 v72, v72, v73, v77
	v_div_fixup_f32 v0, v72, v3, v0
	v_or_b32_e32 v72, 0x800, v92
	v_mov_b32_e32 v73, v93
	v_cvt_pk_bf16_f32 v0, v0, v1
	v_lshl_add_u64 v[72:73], v[102:103], 0, v[72:73]
	global_store_short v[72:73], v0, off
	v_add_f32_e32 v0, v180, v78
	v_max_f32_e32 v3, v90, v90
	v_max_f32_e64 v72, |v86|, |v86|
	v_fma_f32 v0, v0, v82, v74
	v_max_f32_e32 v3, v72, v3
	v_div_scale_f32 v72, s[80:81], v3, v3, v0
	v_rcp_f32_e32 v73, v72
	s_nop 0
	v_fma_f32 v74, -v72, v73, 1.0
	v_fmac_f32_e32 v73, v74, v73
	v_div_scale_f32 v74, vcc, v0, v3, v0
	v_mul_f32_e32 v76, v74, v73
	v_fma_f32 v77, -v72, v76, v74
	v_fmac_f32_e32 v76, v77, v73
	v_fma_f32 v72, -v72, v76, v74
	v_div_fmas_f32 v72, v72, v73, v76
	v_div_fixup_f32 v0, v72, v3, v0
	v_or_b32_e32 v72, 0x1000, v92
	v_mov_b32_e32 v73, v93
	v_cvt_pk_bf16_f32 v0, v0, v1
	v_lshl_add_u64 v[72:73], v[102:103], 0, v[72:73]
	global_store_short v[72:73], v0, off
	v_add_f32_e32 v0, v179, v79
	v_fmac_f32_e32 v75, v0, v83
	v_max_f32_e32 v0, v91, v91
	v_max_f32_e64 v3, |v87|, |v87|
	v_max_f32_e32 v0, v3, v0
	v_div_scale_f32 v3, s[80:81], v0, v0, v75
	v_rcp_f32_e32 v72, v3
	v_or_b32_e32 v92, 0x1800, v92
	v_fma_f32 v73, -v3, v72, 1.0
	v_fmac_f32_e32 v72, v73, v72
	v_div_scale_f32 v73, vcc, v75, v0, v75
	v_mul_f32_e32 v74, v73, v72
	v_fma_f32 v76, -v3, v74, v73
	v_fmac_f32_e32 v74, v76, v72
	v_fma_f32 v3, -v3, v74, v73
	v_div_fmas_f32 v3, v3, v72, v74
	v_div_fixup_f32 v0, v3, v0, v75
	v_cvt_pk_bf16_f32 v0, v0, v1
	v_lshl_add_u64 v[72:73], v[102:103], 0, v[92:93]
	global_store_short v[72:73], v0, off
	s_waitcnt lgkmcnt(0)
	v_cvt_pk_bf16_f32 v226, v214, v216
	v_cvt_pk_bf16_f32 v227, v218, v220
	v_cvt_pk_bf16_f32 v228, v215, v217
	v_cvt_pk_bf16_f32 v229, v219, v221
	v_cvt_pk_bf16_f32 v194, v198, v200
	v_cvt_pk_bf16_f32 v195, v202, v204
	v_cvt_pk_bf16_f32 v196, v199, v201
	v_cvt_pk_bf16_f32 v197, v203, v205
	v_mov_b32_e32 v223, v222
	v_pk_mul_f32 v[68:69], v[68:69], v[222:223]
	v_pk_mul_f32 v[70:71], v[70:71], v[222:223]
	v_pk_mul_f32 v[64:65], v[64:65], v[222:223]
	v_pk_mul_f32 v[66:67], v[66:67], v[222:223]
	v_pk_mul_f32 v[56:57], v[56:57], v[222:223]
	v_pk_mul_f32 v[58:59], v[58:59], v[222:223]
	v_pk_mul_f32 v[60:61], v[60:61], v[222:223]
	v_pk_mul_f32 v[62:63], v[62:63], v[222:223]
	v_pk_mul_f32 v[48:49], v[48:49], v[222:223]
	v_pk_mul_f32 v[50:51], v[50:51], v[222:223]
	v_pk_mul_f32 v[52:53], v[52:53], v[222:223]
	v_pk_mul_f32 v[54:55], v[54:55], v[222:223]
	v_pk_mul_f32 v[40:41], v[40:41], v[222:223]
	v_pk_mul_f32 v[42:43], v[42:43], v[222:223]
	v_pk_mul_f32 v[44:45], v[44:45], v[222:223]
	v_pk_mul_f32 v[46:47], v[46:47], v[222:223]
	ds_read_b64_tr_b16 v[244:245], v224 offset:96
	ds_read_b64_tr_b16 v[246:247], v224 offset:624
	ds_read_b64_tr_b16 v[184:185], v224 offset:128
	ds_read_b64_tr_b16 v[186:187], v224 offset:656
	ds_read_b64_tr_b16 v[188:189], v224 offset:160
	ds_read_b64_tr_b16 v[190:191], v224 offset:688
	s_waitcnt lgkmcnt(10)
	v_mfma_f32_16x16x32_bf16 v[68:71], v[232:235], v[210:213], v[68:71]
	ds_read_b64_tr_b16 v[232:233], v224 offset:192
	ds_read_b64_tr_b16 v[234:235], v224 offset:720
	s_waitcnt lgkmcnt(10)
	v_mfma_f32_16x16x32_bf16 v[64:67], v[236:239], v[210:213], v[64:67]
	ds_read_b64_tr_b16 v[236:237], v224 offset:224
	ds_read_b64_tr_b16 v[238:239], v224 offset:752
	s_waitcnt lgkmcnt(10)
	v_mfma_f32_16x16x32_bf16 v[56:59], v[240:243], v[210:213], v[56:59]
	ds_read_b64_tr_b16 v[240:241], v225
	ds_read_b64_tr_b16 v[242:243], v225 offset:528
	s_waitcnt lgkmcnt(10)
	v_mfma_f32_16x16x32_bf16 v[60:63], v[244:247], v[210:213], v[60:63]
	ds_read_b64_tr_b16 v[244:245], v225 offset:32
	ds_read_b64_tr_b16 v[246:247], v225 offset:560
	s_waitcnt lgkmcnt(10)
	v_mfma_f32_16x16x32_bf16 v[48:51], v[184:187], v[210:213], v[48:51]
	ds_read_b64_tr_b16 v[184:185], v224 offset:16896
	ds_read_b64_tr_b16 v[186:187], v224 offset:17424
	s_waitcnt lgkmcnt(10)
	v_mfma_f32_16x16x32_bf16 v[52:55], v[188:191], v[210:213], v[52:55]
	ds_read_b64_tr_b16 v[188:189], v224 offset:16928
	ds_read_b64_tr_b16 v[190:191], v224 offset:17456
	s_waitcnt lgkmcnt(10)
	v_mfma_f32_16x16x32_bf16 v[40:43], v[232:235], v[210:213], v[40:43]
	ds_read_b64_tr_b16 v[232:233], v224 offset:16960
	ds_read_b64_tr_b16 v[234:235], v224 offset:17488
	s_waitcnt lgkmcnt(10)
	v_mfma_f32_16x16x32_bf16 v[44:47], v[236:239], v[210:213], v[44:47]
	ds_read_b64_tr_b16 v[236:237], v224 offset:16992
	ds_read_b64_tr_b16 v[238:239], v224 offset:17520
	s_waitcnt lgkmcnt(10)
	v_mfma_f32_16x16x32_bf16 v[72:75], v[240:243], v[226:229], 0
	ds_read_b64_tr_b16 v[240:241], v224 offset:17024
	ds_read_b64_tr_b16 v[242:243], v224 offset:17552
	s_waitcnt lgkmcnt(10)
	v_mfma_f32_16x16x32_bf16 v[76:79], v[244:247], v[226:229], 0
	ds_read_b64_tr_b16 v[244:245], v224 offset:17056
	ds_read_b64_tr_b16 v[246:247], v224 offset:17584
	s_waitcnt lgkmcnt(10)
	v_mfma_f32_16x16x32_bf16 v[68:71], v[184:187], v[206:209], v[68:71]
	ds_read_b64_tr_b16 v[184:185], v224 offset:17088
	ds_read_b64_tr_b16 v[186:187], v224 offset:17616
	s_waitcnt lgkmcnt(10)
	v_mfma_f32_16x16x32_bf16 v[64:67], v[188:191], v[206:209], v[64:67]
	ds_read_b64_tr_b16 v[188:189], v224 offset:17120
	ds_read_b64_tr_b16 v[190:191], v224 offset:17648
	s_waitcnt lgkmcnt(10)
	v_mfma_f32_16x16x32_bf16 v[56:59], v[232:235], v[206:209], v[56:59]
	ds_read_b64_tr_b16 v[232:233], v225 offset:16896
	ds_read_b64_tr_b16 v[234:235], v225 offset:17424
	s_waitcnt lgkmcnt(10)
	v_mfma_f32_16x16x32_bf16 v[60:63], v[236:239], v[206:209], v[60:63]
	ds_read_b64_tr_b16 v[236:237], v225 offset:16928
	ds_read_b64_tr_b16 v[238:239], v225 offset:17456
	s_waitcnt lgkmcnt(10)
	v_mfma_f32_16x16x32_bf16 v[48:51], v[240:243], v[206:209], v[48:51]
	s_waitcnt lgkmcnt(8)
	v_mfma_f32_16x16x32_bf16 v[52:55], v[244:247], v[206:209], v[52:55]
	s_waitcnt lgkmcnt(6)
	v_mfma_f32_16x16x32_bf16 v[40:43], v[184:187], v[206:209], v[40:43]
	s_waitcnt lgkmcnt(4)
	v_mfma_f32_16x16x32_bf16 v[44:47], v[188:191], v[206:209], v[44:47]
	s_waitcnt lgkmcnt(2)
	v_mfma_f32_16x16x32_bf16 v[72:75], v[232:235], v[194:197], v[72:75]
	s_waitcnt lgkmcnt(0)
	v_mfma_f32_16x16x32_bf16 v[76:79], v[236:239], v[194:197], v[76:79]
	s_mov_b32 s99, 64
	s_and_b64 vcc, exec, s[62:63]
	s_cselect_b32 s99, 0, s99
	s_or_b64 vcc, s[30:31], s[34:35]
	s_and_b64 vcc, exec, vcc
	s_cselect_b32 s98, 32, 0
	s_or_b32 s99, s99, s98
	s_and_saveexec_b64 s[80:81], s[60:61]
	s_cbranch_execz .LBB0_725
	v_xor_b32_e32 v88, s99, v154
	v_add_u32_e32 v89, 64, v154
	v_xor_b32_e32 v89, s99, v89
	ds_read_b128 v[80:83], v88
	ds_read_b128 v[84:87], v89
	s_nop 7
	s_waitcnt lgkmcnt(1)
	v_pk_fma_f32 v[74:75], v[222:223], v[82:83], v[74:75]
	v_pk_fma_f32 v[72:73], v[222:223], v[80:81], v[72:73]
	s_waitcnt lgkmcnt(0)
	v_pk_fma_f32 v[78:79], v[222:223], v[86:87], v[78:79]
	v_pk_fma_f32 v[76:77], v[222:223], v[84:85], v[76:77]
	ds_write_b128 v88, v[72:75]
	ds_write_b128 v89, v[76:79]
	s_branch .LBB0_725
